# router: the four group-logit wave reductions interleaved level by level; expert-weight LDS reads addressed from one base register with immediate offsets
# speedup vs baseline: 1.0103x; 1.0026x over previous
; __device__ __forceinline__ void router_ph(const int WID_, const bf16* __restrict__ x3, const float* __restrict__ nw, const float* __restrict__ wrg, const float* __restrict__ brg, ...
;     ...
;         float h[16]; float s = 0.f;
; #pragma unroll
;         for (int j = 0; j < 2; ++j) { const unsigned wd[4] = {nx[j].x, nx[j].y, nx[j].z, nx[j].w};
; #pragma unroll
;             for (int q = 0; q < 4; ++q) { const float lo = __builtin_bit_cast(float, wd[q] << 16), hi = __builtin_bit_cast(float, wd[q] & 0xffff0000u); h[8 * j + 2 * q] = lo; h[8 * j + 2 * q + 1] = hi; s += lo * lo + hi * hi; } }
;         { const int mn = min(m + 8, tile * 256 + 248 + wv); const uint4* xr = (const uint4*)(x3 + (size_t)mn * D);
; #pragma unroll
;           for (int j = 0; j < 2; ++j) nx[j] = xr[lane + 64 * j]; }
;         s = wave_sum(s);
;         const float rs = rsqrtf(s * (1.f / D) + 1e-6f);
;         float l1[4] = {0.f, 0.f, 0.f, 0.f};
; #pragma unroll
;         for (int j = 0; j < 2; ++j) {
;             const int k0 = (lane + 64 * j) * 8;
;             const float4 ga = gw[2 * j], gb = gw[2 * j + 1];
;             h[8 * j] *= rs * ga.x; h[8 * j + 1] *= rs * ga.y; h[8 * j + 2] *= rs * ga.z; h[8 * j + 3] *= rs * ga.w;
;             h[8 * j + 4] *= rs * gb.x; h[8 * j + 5] *= rs * gb.y; h[8 * j + 6] *= rs * gb.z; h[8 * j + 7] *= rs * gb.w;
; #pragma unroll
;             for (int e = 0; e < 8; ++e) { const h4 w = *(const h4*)(wg16 + (k0 + e) * 4); const float x = h[8 * j + e];
;                 l1[0] += x * (float)w[0]; l1[1] += x * (float)w[1]; l1[2] += x * (float)w[2]; l1[3] += x * (float)w[3]; }
.LBB0_2145:
	v_and_b32_e32 v90, 0xffff0000, v16
	v_and_b32_e32 v92, 0xffff0000, v17
	v_lshlrev_b32_e32 v59, 16, v16
	v_mul_f32_e32 v14, v90, v90
	v_lshlrev_b32_e32 v91, 16, v17
	v_mul_f32_e32 v16, v92, v92
	v_fmac_f32_e32 v14, v59, v59
	v_fmac_f32_e32 v16, v91, v91
	v_and_b32_e32 v94, 0xffff0000, v18
	v_add_f32_e32 v14, v16, v14
	v_lshlrev_b32_e32 v93, 16, v18
	v_mul_f32_e32 v16, v94, v94
	v_fmac_f32_e32 v16, v93, v93
	v_and_b32_e32 v96, 0xffff0000, v19
	v_add_f32_e32 v14, v16, v14
	v_lshlrev_b32_e32 v95, 16, v19
	v_mul_f32_e32 v16, v96, v96
	v_and_b32_e32 v85, 0xffff0000, v13
	v_and_b32_e32 v84, 0xffff0000, v12
	v_fmac_f32_e32 v16, v95, v95
	v_lshlrev_b32_e32 v27, 16, v13
	v_lshlrev_b32_e32 v26, 16, v12
	v_pk_mul_f32 v[12:13], v[84:85], v[84:85]
	v_add_f32_e32 v14, v16, v14
	v_pk_fma_f32 v[16:17], v[26:27], v[26:27], v[12:13]
	v_and_b32_e32 v86, 0xffff0000, v2
	v_add_f32_e32 v14, v16, v14
	v_add_f32_e32 v88, v17, v14
	v_and_b32_e32 v14, 0xffff0000, v15
	v_lshlrev_b32_e32 v15, 16, v15
	v_lshlrev_b32_e32 v87, 16, v2
	v_mov_b32_e32 v82, v14
	v_mov_b32_e32 v83, v86
	v_mov_b32_e32 v80, v15
	v_mov_b32_e32 v81, v87
	v_pk_mul_f32 v[82:83], v[82:83], v[82:83]
	s_add_i32 s4, s44, 16
	v_pk_fma_f32 v[80:81], v[80:81], v[80:81], v[82:83]
	s_min_i32 s4, s4, s33
	v_add_f32_e32 v2, v81, v88
	v_add_f32_e32 v2, v80, v2
	v_mov_b32_e32 v80, 0
	s_ashr_i32 s5, s4, 31
	v_add_f32_dpp v2, v2, v2 quad_perm:[1,0,3,2] row_mask:0xf bank_mask:0xf bound_ctrl:1
	s_lshl_b64 s[4:5], s[4:5], 11
	v_lshl_add_u64 v[12:13], v[10:11], 0, s[4:5]
	v_add_f32_dpp v2, v2, v2 quad_perm:[2,3,0,1] row_mask:0xf bank_mask:0xf bound_ctrl:1
	ds_read_b128 v[16:19], v21 offset:256
	ds_read_b128 v[22:25], v52 offset:256
	ds_read_b128 v[60:63], v53 offset:256
	ds_read_b128 v[64:67], v54 offset:256
	ds_read_b128 v[68:71], v55 offset:256
	ds_read_b128 v[72:75], v56 offset:256
	ds_read_b128 v[76:79], v57 offset:256
	v_add_f32_dpp v2, v2, v2 row_half_mirror row_mask:0xf bank_mask:0xf bound_ctrl:1
	s_add_i32 s5, 0, 0x12100
	s_waitcnt lgkmcnt(0)
	v_cvt_f32_f16_sdwa v89, v77 dst_sel:DWORD dst_unused:UNUSED_PAD src0_sel:WORD_1
	v_add_f32_dpp v2, v2, v2 row_mirror row_mask:0xf bank_mask:0xf bound_ctrl:1
	v_cvt_f32_f16_sdwa v88, v79 dst_sel:DWORD dst_unused:UNUSED_PAD src0_sel:WORD_1
	s_nop 0
	v_mov_b32_dpp v80, v2 row_bcast:15 row_mask:0xa bank_mask:0xf
	v_add_f32_e32 v2, v2, v80
	v_mov_b32_e32 v80, 0
	s_nop 1
	v_mov_b32_dpp v80, v2 row_bcast:31 row_mask:0xc bank_mask:0xf
	v_add_f32_e32 v2, v2, v80
	s_nop 0
	v_readlane_b32 s4, v2, 63
	s_nop 1
	v_fma_f32 v2, s4, v196, v194
	v_mul_f32_e32 v80, 0x4b800000, v2
	v_cmp_gt_f32_e32 vcc, s64, v2
	s_nop 1
	v_cndmask_b32_e32 v2, v2, v80, vcc
	v_rsq_f32_e32 v2, v2
	ds_read_b128 v[80:83], v58 offset:256
	v_mul_f32_e32 v97, 0x45800000, v2
	v_cndmask_b32_e32 v2, v2, v97, vcc
	v_mul_f32_e32 v97, v29, v2
	v_mul_f32_e32 v97, v97, v59
	v_mul_f32_e32 v59, v31, v2
	v_mul_f32_e32 v90, v59, v90
	v_mul_f32_e32 v59, v30, v2
	v_mul_f32_e32 v91, v59, v91
	v_mul_f32_e32 v59, v3, v2
	v_mul_f32_e32 v92, v59, v92
	v_mul_f32_e32 v59, v33, v2
	v_mul_f32_e32 v93, v59, v93
	v_mul_f32_e32 v59, v32, v2
	v_mul_f32_e32 v94, v59, v94
	v_mul_f32_e32 v59, v6, v2
	v_mul_f32_e32 v95, v59, v95
	v_mul_f32_e32 v59, v7, v2
	v_mul_f32_e32 v96, v59, v96
	v_fma_mix_f32 v59, v97, v16, 0 op_sel_hi:[0,1,0]
	v_fma_mix_f32 v16, v97, v16, 0 op_sel:[0,1,0] op_sel_hi:[0,1,0]
	v_fma_mix_f32 v16, v90, v18, v16 op_sel:[0,1,0] op_sel_hi:[0,1,0]
	v_fma_mix_f32 v16, v91, v22, v16 op_sel:[0,1,0] op_sel_hi:[0,1,0]
	v_fma_mix_f32 v16, v92, v24, v16 op_sel:[0,1,0] op_sel_hi:[0,1,0]
	v_fma_mix_f32 v98, v97, v17, 0 op_sel_hi:[0,1,0]
	v_fma_mix_f32 v17, v97, v17, 0 op_sel:[0,1,0] op_sel_hi:[0,1,0]
	v_fma_mix_f32 v16, v93, v60, v16 op_sel:[0,1,0] op_sel_hi:[0,1,0]
	v_fma_mix_f32 v17, v90, v19, v17 op_sel:[0,1,0] op_sel_hi:[0,1,0]
	v_fma_mix_f32 v16, v94, v62, v16 op_sel:[0,1,0] op_sel_hi:[0,1,0]
	v_fma_mix_f32 v59, v90, v18, v59 op_sel_hi:[0,1,0]
	v_fma_mix_f32 v17, v91, v23, v17 op_sel:[0,1,0] op_sel_hi:[0,1,0]
	v_fma_mix_f32 v16, v95, v64, v16 op_sel:[0,1,0] op_sel_hi:[0,1,0]
	v_fma_mix_f32 v18, v90, v19, v98 op_sel_hi:[0,1,0]
	v_fma_mix_f32 v19, v91, v22, v59 op_sel_hi:[0,1,0]
	v_fma_mix_f32 v17, v92, v25, v17 op_sel:[0,1,0] op_sel_hi:[0,1,0]
	v_fma_mix_f32 v22, v96, v66, v16 op_sel:[0,1,0] op_sel_hi:[0,1,0]
	v_mul_f32_e32 v16, v8, v2
	v_fma_mix_f32 v18, v91, v23, v18 op_sel_hi:[0,1,0]
	v_fma_mix_f32 v19, v92, v24, v19 op_sel_hi:[0,1,0]
	v_fma_mix_f32 v17, v93, v61, v17 op_sel:[0,1,0] op_sel_hi:[0,1,0]
	v_mul_f32_e32 v98, v16, v26
	v_mul_f32_e32 v16, v9, v2
	v_fma_mix_f32 v18, v92, v25, v18 op_sel_hi:[0,1,0]
	v_fma_mix_f32 v19, v93, v60, v19 op_sel_hi:[0,1,0]
	v_fma_mix_f32 v17, v94, v63, v17 op_sel:[0,1,0] op_sel_hi:[0,1,0]
	v_mul_f32_e32 v84, v16, v84
	v_mul_f32_e32 v16, v35, v2
	v_fma_mix_f32 v18, v93, v61, v18 op_sel_hi:[0,1,0]
	v_fma_mix_f32 v19, v94, v62, v19 op_sel_hi:[0,1,0]
	v_fma_mix_f32 v17, v95, v65, v17 op_sel:[0,1,0] op_sel_hi:[0,1,0]
	v_mul_f32_e32 v99, v16, v27
	v_mul_f32_e32 v16, v34, v2
	v_fma_mix_f32 v18, v94, v63, v18 op_sel_hi:[0,1,0]
	v_fma_mix_f32 v19, v95, v64, v19 op_sel_hi:[0,1,0]
	v_fma_mix_f32 v23, v96, v67, v17 op_sel:[0,1,0] op_sel_hi:[0,1,0]
	v_mul_f32_e32 v85, v16, v85
	v_pk_mul_f32 v[16:17], v[0:1], v[2:3] op_sel_hi:[1,0]
	v_fma_mix_f32 v18, v95, v65, v18 op_sel_hi:[0,1,0]
	v_fma_mix_f32 v19, v96, v66, v19 op_sel_hi:[0,1,0]
	v_pk_mul_f32 v[26:27], v[16:17], v[86:87]
	v_pk_mul_f32 v[16:17], v[4:5], v[2:3] op_sel_hi:[1,0]
	v_fma_mix_f32 v18, v96, v67, v18 op_sel_hi:[0,1,0]
	v_pk_mul_f32 v[24:25], v[16:17], v[14:15]
	v_fma_mix_f32 v14, v98, v68, v19 op_sel_hi:[0,1,0]
	v_fma_mix_f32 v15, v98, v68, v22 op_sel:[0,1,0] op_sel_hi:[0,1,0]
	v_fma_mix_f32 v16, v98, v69, v18 op_sel_hi:[0,1,0]
	v_fma_mix_f32 v17, v98, v69, v23 op_sel:[0,1,0] op_sel_hi:[0,1,0]
	v_fma_mix_f32 v14, v84, v70, v14 op_sel_hi:[0,1,0]
	v_fma_mix_f32 v15, v84, v70, v15 op_sel:[0,1,0] op_sel_hi:[0,1,0]
	v_fma_mix_f32 v16, v84, v71, v16 op_sel_hi:[0,1,0]
	v_fma_mix_f32 v17, v84, v71, v17 op_sel:[0,1,0] op_sel_hi:[0,1,0]
	v_fma_mix_f32 v14, v99, v72, v14 op_sel_hi:[0,1,0]
	v_fma_mix_f32 v15, v99, v72, v15 op_sel:[0,1,0] op_sel_hi:[0,1,0]
	v_fma_mix_f32 v16, v99, v73, v16 op_sel_hi:[0,1,0]
	v_fma_mix_f32 v17, v99, v73, v17 op_sel:[0,1,0] op_sel_hi:[0,1,0]
	v_fma_mix_f32 v14, v85, v74, v14 op_sel_hi:[0,1,0]
	v_fma_mix_f32 v22, v85, v74, v15 op_sel:[0,1,0] op_sel_hi:[0,1,0]
	v_fma_mix_f32 v23, v85, v75, v16 op_sel_hi:[0,1,0]
	v_fma_mix_f32 v16, v85, v75, v17 op_sel:[0,1,0] op_sel_hi:[0,1,0]
	v_fma_mix_f32 v18, v27, v76, v14 op_sel_hi:[0,1,0]
	v_pk_mul_f32 v[14:15], v[26:27], v[88:89]
	v_cvt_f32_f16_sdwa v17, v76 dst_sel:DWORD dst_unused:UNUSED_PAD src0_sel:WORD_1
	v_add_f32_e32 v15, v15, v16
	v_cvt_f32_f16_sdwa v16, v78 dst_sel:DWORD dst_unused:UNUSED_PAD src0_sel:WORD_1
	v_fma_mix_f32 v59, v26, v78, v18 op_sel_hi:[0,1,0]
	v_cvt_f32_f16_e32 v19, v77
	v_cvt_f32_f16_e32 v18, v79
	v_pk_mul_f32 v[16:17], v[26:27], v[16:17]
	s_waitcnt lgkmcnt(0)
; __device__ __forceinline__ void router_ph(const int WID_, const bf16* __restrict__ x3, const float* __restrict__ nw, const float* __restrict__ wrg, const float* __restrict__ brg, ...
;     ...
;         for (int i = 0; i < 4; ++i) l1[i] = wave_sum(l1[i]) + brg_l[i];
;         int grp = 0; float best = l1[0];
; #pragma unroll
;         for (int i = 1; i < 4; ++i) if (l1[i] > best) { best = l1[i]; grp = i; }
;         float se = 0.f;
; #pragma unroll
;         for (int i = 0; i < 4; ++i) se += __expf(l1[i] - best);
;         const float g1 = 1.f / se;
;         float l2[8] = {};
;         const _Float16* we = we16 + (size_t)grp * D * 8;
; #pragma unroll
;         for (int j = 0; j < 2; ++j) {
;             const int k0 = (lane + 64 * j) * 8;
; #pragma unroll
;             for (int e = 0; e < 8; ++e) { const float x = h[8 * j + e]; const h8 w = *(const h8*)(we + (k0 + e) * 8);
; #pragma unroll
;                 for (int q = 0; q < 8; ++q) l2[q] += x * (float)w[q]; }
	v_fma_mix_f32 v59, v25, v80, v59 op_sel_hi:[0,1,0]
	v_add_f32_e32 v17, v17, v22
	v_add_f32_e32 v22, v16, v17
	v_pk_mul_f32 v[16:17], v[26:27], v[18:19]
	v_cvt_f32_f16_sdwa v19, v81 dst_sel:DWORD dst_unused:UNUSED_PAD src0_sel:WORD_1
	v_cvt_f32_f16_sdwa v18, v83 dst_sel:DWORD dst_unused:UNUSED_PAD src0_sel:WORD_1
	v_add_f32_e32 v17, v17, v23
	v_add_f32_e32 v23, v16, v17
	v_add_f32_e32 v16, v14, v15
	v_pk_mul_f32 v[14:15], v[24:25], v[18:19]
	v_cvt_f32_f16_sdwa v17, v80 dst_sel:DWORD dst_unused:UNUSED_PAD src0_sel:WORD_1
	v_add_f32_e32 v15, v15, v16
	v_cvt_f32_f16_sdwa v16, v82 dst_sel:DWORD dst_unused:UNUSED_PAD src0_sel:WORD_1
	v_cvt_f32_f16_e32 v19, v81
	v_cvt_f32_f16_e32 v18, v83
	v_fma_mix_f32 v59, v24, v82, v59 op_sel_hi:[0,1,0]
	v_pk_mul_f32 v[16:17], v[24:25], v[16:17]
	s_nop 0
	v_add_f32_e32 v17, v17, v22
	v_add_f32_e32 v22, v16, v17
	v_pk_mul_f32 v[16:17], v[24:25], v[18:19]
	v_add_f32_e32 v19, v14, v15
	v_add_f32_e32 v17, v17, v23
	v_add_f32_e32 v18, v16, v17
	v_mov_b32_e32 v14, s5
	ds_read_b128 v[100:103], v14
	v_add_f32_dpp v59, v59, v59 quad_perm:[1,0,3,2] row_mask:0xf bank_mask:0xf bound_ctrl:1
	v_add_f32_dpp v22, v22, v22 quad_perm:[1,0,3,2] row_mask:0xf bank_mask:0xf bound_ctrl:1
	v_add_f32_dpp v18, v18, v18 quad_perm:[1,0,3,2] row_mask:0xf bank_mask:0xf bound_ctrl:1
	v_add_f32_dpp v19, v19, v19 quad_perm:[1,0,3,2] row_mask:0xf bank_mask:0xf bound_ctrl:1
	v_add_f32_dpp v59, v59, v59 quad_perm:[2,3,0,1] row_mask:0xf bank_mask:0xf bound_ctrl:1
	v_add_f32_dpp v22, v22, v22 quad_perm:[2,3,0,1] row_mask:0xf bank_mask:0xf bound_ctrl:1
	v_add_f32_dpp v18, v18, v18 quad_perm:[2,3,0,1] row_mask:0xf bank_mask:0xf bound_ctrl:1
	v_add_f32_dpp v19, v19, v19 quad_perm:[2,3,0,1] row_mask:0xf bank_mask:0xf bound_ctrl:1
	v_add_f32_dpp v59, v59, v59 row_half_mirror row_mask:0xf bank_mask:0xf bound_ctrl:1
	v_add_f32_dpp v22, v22, v22 row_half_mirror row_mask:0xf bank_mask:0xf bound_ctrl:1
	v_add_f32_dpp v18, v18, v18 row_half_mirror row_mask:0xf bank_mask:0xf bound_ctrl:1
	v_add_f32_dpp v19, v19, v19 row_half_mirror row_mask:0xf bank_mask:0xf bound_ctrl:1
	v_add_f32_dpp v59, v59, v59 row_mirror row_mask:0xf bank_mask:0xf bound_ctrl:1
	v_add_f32_dpp v22, v22, v22 row_mirror row_mask:0xf bank_mask:0xf bound_ctrl:1
	v_add_f32_dpp v18, v18, v18 row_mirror row_mask:0xf bank_mask:0xf bound_ctrl:1
	v_add_f32_dpp v19, v19, v19 row_mirror row_mask:0xf bank_mask:0xf bound_ctrl:1
	v_mov_b32_e32 v104, 0
	v_mov_b32_e32 v105, 0
	v_mov_b32_e32 v106, 0
	v_mov_b32_e32 v107, 0
	v_mov_b32_dpp v104, v59 row_bcast:15 row_mask:0xa bank_mask:0xf
	v_mov_b32_dpp v105, v22 row_bcast:15 row_mask:0xa bank_mask:0xf
	v_mov_b32_dpp v106, v18 row_bcast:15 row_mask:0xa bank_mask:0xf
	v_mov_b32_dpp v107, v19 row_bcast:15 row_mask:0xa bank_mask:0xf
	v_add_f32_e32 v59, v59, v104
	v_add_f32_e32 v22, v22, v105
	v_add_f32_e32 v18, v18, v106
	v_add_f32_e32 v19, v19, v107
	v_mov_b32_e32 v104, 0
	v_mov_b32_e32 v105, 0
	v_mov_b32_e32 v106, 0
	v_mov_b32_e32 v107, 0
	v_mov_b32_dpp v104, v59 row_bcast:31 row_mask:0xc bank_mask:0xf
	v_mov_b32_dpp v105, v22 row_bcast:31 row_mask:0xc bank_mask:0xf
	v_mov_b32_dpp v106, v18 row_bcast:31 row_mask:0xc bank_mask:0xf
	v_mov_b32_dpp v107, v19 row_bcast:31 row_mask:0xc bank_mask:0xf
	v_add_f32_e32 v59, v59, v104
	v_add_f32_e32 v22, v22, v105
	v_add_f32_e32 v18, v18, v106
	v_add_f32_e32 v19, v19, v107
	v_readlane_b32 s4, v59, 63
	v_readlane_b32 s5, v22, 63
	v_readlane_b32 s6, v18, 63
	v_readlane_b32 s7, v19, 63
	s_waitcnt lgkmcnt(0)
	v_pk_add_f32 v[22:23], s[4:5], v[100:101]
	v_add_f32_e32 v59, s6, v102
	v_add_f32_e32 v60, s7, v103
	v_cmp_gt_f32_e64 s[4:5], v23, v22
	s_nop 1
	v_cndmask_b32_e64 v14, v22, v23, s[4:5]
	v_cmp_gt_f32_e64 s[6:7], v59, v14
	s_nop 1
	v_cndmask_b32_e64 v61, v14, v59, s[6:7]
	v_cndmask_b32_e64 v14, 0, 1, s[4:5]
	s_and_b64 s[4:5], s[6:7], exec
	v_cmp_gt_f32_e32 vcc, v60, v61
	v_readfirstlane_b32 s4, v14
	s_cselect_b32 s6, 2, s4
	s_and_b64 s[4:5], vcc, exec
	s_cselect_b32 s49, 3, s6
	s_lshl_b32 s4, s49, 14
	s_add_i32 s48, s4, 0
	global_load_dwordx4 v[16:19], v[12:13], off
	s_nop 0
	global_load_dwordx4 v[12:15], v[12:13], off offset:1024
	v_add_u32_e32 v112, s48, v36
	ds_read_b128 v[132:135], v112 offset:8448
	ds_read_b128 v[136:139], v112 offset:9472
	ds_read_b128 v[140:143], v112 offset:10496
	ds_read_b128 v[144:147], v112 offset:11520
	ds_read_b128 v[148:151], v112 offset:12544
	ds_read_b128 v[152:155], v112 offset:13568
	ds_read_b128 v[156:159], v112 offset:14592
	ds_read_b128 v[160:163], v112 offset:15616
	ds_read_b128 v[164:167], v112 offset:16640
	ds_read_b128 v[168:171], v112 offset:17664
	ds_read_b128 v[172:175], v112 offset:18688
	ds_read_b128 v[176:179], v112 offset:19712
	s_waitcnt lgkmcnt(11)
	v_fma_mix_f32 v70, v97, v132, 0 op_sel_hi:[0,1,0]
	v_fma_mix_f32 v71, v97, v132, 0 op_sel:[0,1,0] op_sel_hi:[0,1,0]
	v_fma_mix_f32 v72, v97, v133, 0 op_sel_hi:[0,1,0]
	v_fma_mix_f32 v73, v97, v133, 0 op_sel:[0,1,0] op_sel_hi:[0,1,0]
	v_fma_mix_f32 v74, v97, v134, 0 op_sel_hi:[0,1,0]
	v_fma_mix_f32 v75, v97, v134, 0 op_sel:[0,1,0] op_sel_hi:[0,1,0]
	v_fma_mix_f32 v76, v97, v135, 0 op_sel_hi:[0,1,0]
	v_fma_mix_f32 v77, v97, v135, 0 op_sel:[0,1,0] op_sel_hi:[0,1,0]
	s_waitcnt lgkmcnt(10)
	v_fma_mix_f32 v70, v90, v136, v70 op_sel_hi:[0,1,0]
	v_fma_mix_f32 v71, v90, v136, v71 op_sel:[0,1,0] op_sel_hi:[0,1,0]
	v_fma_mix_f32 v72, v90, v137, v72 op_sel_hi:[0,1,0]
	v_fma_mix_f32 v73, v90, v137, v73 op_sel:[0,1,0] op_sel_hi:[0,1,0]
	v_fma_mix_f32 v74, v90, v138, v74 op_sel_hi:[0,1,0]
	v_fma_mix_f32 v75, v90, v138, v75 op_sel:[0,1,0] op_sel_hi:[0,1,0]
	v_fma_mix_f32 v76, v90, v139, v76 op_sel_hi:[0,1,0]
	v_fma_mix_f32 v77, v90, v139, v77 op_sel:[0,1,0] op_sel_hi:[0,1,0]
	s_waitcnt lgkmcnt(9)
; __device__ __forceinline__ void router_ph(const int WID_, const bf16* __restrict__ x3, const float* __restrict__ nw, const float* __restrict__ wrg, const float* __restrict__ brg, ...
;     ...
;             for (int e = 0; e < 8; ++e) { const float x = h[8 * j + e]; const h8 w = *(const h8*)(we + (k0 + e) * 8);
; #pragma unroll
;                 for (int q = 0; q < 8; ++q) l2[q] += x * (float)w[q]; }
	v_fma_mix_f32 v70, v91, v140, v70 op_sel_hi:[0,1,0]
	v_fma_mix_f32 v71, v91, v140, v71 op_sel:[0,1,0] op_sel_hi:[0,1,0]
	v_fma_mix_f32 v72, v91, v141, v72 op_sel_hi:[0,1,0]
	v_fma_mix_f32 v73, v91, v141, v73 op_sel:[0,1,0] op_sel_hi:[0,1,0]
	v_fma_mix_f32 v74, v91, v142, v74 op_sel_hi:[0,1,0]
	v_fma_mix_f32 v75, v91, v142, v75 op_sel:[0,1,0] op_sel_hi:[0,1,0]
	v_fma_mix_f32 v76, v91, v143, v76 op_sel_hi:[0,1,0]
	v_fma_mix_f32 v77, v91, v143, v77 op_sel:[0,1,0] op_sel_hi:[0,1,0]
	s_waitcnt lgkmcnt(8)
	v_fma_mix_f32 v70, v92, v144, v70 op_sel_hi:[0,1,0]
	v_fma_mix_f32 v71, v92, v144, v71 op_sel:[0,1,0] op_sel_hi:[0,1,0]
	v_fma_mix_f32 v72, v92, v145, v72 op_sel_hi:[0,1,0]
	v_fma_mix_f32 v73, v92, v145, v73 op_sel:[0,1,0] op_sel_hi:[0,1,0]
	v_fma_mix_f32 v74, v92, v146, v74 op_sel_hi:[0,1,0]
	v_fma_mix_f32 v75, v92, v146, v75 op_sel:[0,1,0] op_sel_hi:[0,1,0]
	v_fma_mix_f32 v76, v92, v147, v76 op_sel_hi:[0,1,0]
	v_fma_mix_f32 v77, v92, v147, v77 op_sel:[0,1,0] op_sel_hi:[0,1,0]
	ds_read_b128 v[180:183], v112 offset:20736
	ds_read_b128 v[184:187], v112 offset:21760
	ds_read_b128 v[188:191], v112 offset:22784
	ds_read_b128 v[108:111], v112 offset:23808
	s_waitcnt lgkmcnt(11)
	v_fma_mix_f32 v70, v93, v148, v70 op_sel_hi:[0,1,0]
	v_fma_mix_f32 v71, v93, v148, v71 op_sel:[0,1,0] op_sel_hi:[0,1,0]
	v_fma_mix_f32 v72, v93, v149, v72 op_sel_hi:[0,1,0]
	v_fma_mix_f32 v73, v93, v149, v73 op_sel:[0,1,0] op_sel_hi:[0,1,0]
	v_fma_mix_f32 v74, v93, v150, v74 op_sel_hi:[0,1,0]
	v_fma_mix_f32 v75, v93, v150, v75 op_sel:[0,1,0] op_sel_hi:[0,1,0]
	v_fma_mix_f32 v76, v93, v151, v76 op_sel_hi:[0,1,0]
	v_fma_mix_f32 v77, v93, v151, v77 op_sel:[0,1,0] op_sel_hi:[0,1,0]
	s_waitcnt lgkmcnt(10)
	v_fma_mix_f32 v70, v94, v152, v70 op_sel_hi:[0,1,0]
	v_fma_mix_f32 v71, v94, v152, v71 op_sel:[0,1,0] op_sel_hi:[0,1,0]
	v_fma_mix_f32 v72, v94, v153, v72 op_sel_hi:[0,1,0]
	v_fma_mix_f32 v73, v94, v153, v73 op_sel:[0,1,0] op_sel_hi:[0,1,0]
	v_fma_mix_f32 v74, v94, v154, v74 op_sel_hi:[0,1,0]
	v_fma_mix_f32 v75, v94, v154, v75 op_sel:[0,1,0] op_sel_hi:[0,1,0]
	v_fma_mix_f32 v76, v94, v155, v76 op_sel_hi:[0,1,0]
	v_fma_mix_f32 v77, v94, v155, v77 op_sel:[0,1,0] op_sel_hi:[0,1,0]
	s_waitcnt lgkmcnt(9)
	v_fma_mix_f32 v70, v95, v156, v70 op_sel_hi:[0,1,0]
	v_fma_mix_f32 v71, v95, v156, v71 op_sel:[0,1,0] op_sel_hi:[0,1,0]
	v_fma_mix_f32 v72, v95, v157, v72 op_sel_hi:[0,1,0]
	v_fma_mix_f32 v73, v95, v157, v73 op_sel:[0,1,0] op_sel_hi:[0,1,0]
	v_fma_mix_f32 v74, v95, v158, v74 op_sel_hi:[0,1,0]
	v_fma_mix_f32 v75, v95, v158, v75 op_sel:[0,1,0] op_sel_hi:[0,1,0]
	v_fma_mix_f32 v76, v95, v159, v76 op_sel_hi:[0,1,0]
	v_fma_mix_f32 v77, v95, v159, v77 op_sel:[0,1,0] op_sel_hi:[0,1,0]
	s_waitcnt lgkmcnt(8)
	v_fma_mix_f32 v70, v96, v160, v70 op_sel_hi:[0,1,0]
	v_fma_mix_f32 v71, v96, v160, v71 op_sel:[0,1,0] op_sel_hi:[0,1,0]
	v_fma_mix_f32 v72, v96, v161, v72 op_sel_hi:[0,1,0]
	v_fma_mix_f32 v73, v96, v161, v73 op_sel:[0,1,0] op_sel_hi:[0,1,0]
	v_fma_mix_f32 v74, v96, v162, v74 op_sel_hi:[0,1,0]
	v_fma_mix_f32 v75, v96, v162, v75 op_sel:[0,1,0] op_sel_hi:[0,1,0]
	v_fma_mix_f32 v76, v96, v163, v76 op_sel_hi:[0,1,0]
	v_fma_mix_f32 v77, v96, v163, v77 op_sel:[0,1,0] op_sel_hi:[0,1,0]
	s_waitcnt lgkmcnt(7)
	v_fma_mix_f32 v70, v98, v164, v70 op_sel_hi:[0,1,0]
	v_fma_mix_f32 v71, v98, v164, v71 op_sel:[0,1,0] op_sel_hi:[0,1,0]
	v_fma_mix_f32 v72, v98, v165, v72 op_sel_hi:[0,1,0]
	v_fma_mix_f32 v73, v98, v165, v73 op_sel:[0,1,0] op_sel_hi:[0,1,0]
	v_fma_mix_f32 v74, v98, v166, v74 op_sel_hi:[0,1,0]
	v_fma_mix_f32 v75, v98, v166, v75 op_sel:[0,1,0] op_sel_hi:[0,1,0]
	v_fma_mix_f32 v76, v98, v167, v76 op_sel_hi:[0,1,0]
	v_fma_mix_f32 v77, v98, v167, v77 op_sel:[0,1,0] op_sel_hi:[0,1,0]
	s_waitcnt lgkmcnt(6)
	v_fma_mix_f32 v70, v84, v168, v70 op_sel_hi:[0,1,0]
	v_fma_mix_f32 v71, v84, v168, v71 op_sel:[0,1,0] op_sel_hi:[0,1,0]
	v_fma_mix_f32 v72, v84, v169, v72 op_sel_hi:[0,1,0]
	v_fma_mix_f32 v73, v84, v169, v73 op_sel:[0,1,0] op_sel_hi:[0,1,0]
	v_fma_mix_f32 v74, v84, v170, v74 op_sel_hi:[0,1,0]
	v_fma_mix_f32 v75, v84, v170, v75 op_sel:[0,1,0] op_sel_hi:[0,1,0]
	v_fma_mix_f32 v76, v84, v171, v76 op_sel_hi:[0,1,0]
	v_fma_mix_f32 v77, v84, v171, v77 op_sel:[0,1,0] op_sel_hi:[0,1,0]
	s_waitcnt lgkmcnt(5)
	v_fma_mix_f32 v70, v99, v172, v70 op_sel_hi:[0,1,0]
	v_fma_mix_f32 v71, v99, v172, v71 op_sel:[0,1,0] op_sel_hi:[0,1,0]
	v_fma_mix_f32 v72, v99, v173, v72 op_sel_hi:[0,1,0]
	v_fma_mix_f32 v73, v99, v173, v73 op_sel:[0,1,0] op_sel_hi:[0,1,0]
	v_fma_mix_f32 v74, v99, v174, v74 op_sel_hi:[0,1,0]
	v_fma_mix_f32 v75, v99, v174, v75 op_sel:[0,1,0] op_sel_hi:[0,1,0]
	v_fma_mix_f32 v76, v99, v175, v76 op_sel_hi:[0,1,0]
	v_fma_mix_f32 v77, v99, v175, v77 op_sel:[0,1,0] op_sel_hi:[0,1,0]
	s_waitcnt lgkmcnt(4)
	v_fma_mix_f32 v70, v85, v176, v70 op_sel_hi:[0,1,0]
	v_fma_mix_f32 v71, v85, v176, v71 op_sel:[0,1,0] op_sel_hi:[0,1,0]
	v_fma_mix_f32 v72, v85, v177, v72 op_sel_hi:[0,1,0]
	v_fma_mix_f32 v73, v85, v177, v73 op_sel:[0,1,0] op_sel_hi:[0,1,0]
	v_fma_mix_f32 v74, v85, v178, v74 op_sel_hi:[0,1,0]
	v_fma_mix_f32 v75, v85, v178, v75 op_sel:[0,1,0] op_sel_hi:[0,1,0]
	v_fma_mix_f32 v76, v85, v179, v76 op_sel_hi:[0,1,0]
	v_fma_mix_f32 v77, v85, v179, v77 op_sel:[0,1,0] op_sel_hi:[0,1,0]
	s_waitcnt lgkmcnt(3)
	v_fma_mix_f32 v70, v27, v180, v70 op_sel_hi:[0,1,0]
	v_fma_mix_f32 v71, v27, v180, v71 op_sel:[0,1,0] op_sel_hi:[0,1,0]
	v_fma_mix_f32 v72, v27, v181, v72 op_sel_hi:[0,1,0]
	v_fma_mix_f32 v73, v27, v181, v73 op_sel:[0,1,0] op_sel_hi:[0,1,0]
	v_fma_mix_f32 v74, v27, v182, v74 op_sel_hi:[0,1,0]
	v_fma_mix_f32 v75, v27, v182, v75 op_sel:[0,1,0] op_sel_hi:[0,1,0]
	v_fma_mix_f32 v76, v27, v183, v76 op_sel_hi:[0,1,0]
	v_fma_mix_f32 v77, v27, v183, v77 op_sel:[0,1,0] op_sel_hi:[0,1,0]
	s_waitcnt lgkmcnt(2)
; __device__ __forceinline__ void router_ph(const int WID_, const bf16* __restrict__ x3, const float* __restrict__ nw, const float* __restrict__ wrg, const float* __restrict__ brg, ...
;     ...
;             for (int e = 0; e < 8; ++e) { const float x = h[8 * j + e]; const h8 w = *(const h8*)(we + (k0 + e) * 8);
; #pragma unroll
;                 for (int q = 0; q < 8; ++q) l2[q] += x * (float)w[q]; }
;         }
; #pragma unroll
;         for (int i = 0; i < 8; ++i) l2[i] = wave_sum(l2[i]) + bre_l[grp * 8 + i];
	v_fma_mix_f32 v70, v26, v184, v70 op_sel_hi:[0,1,0]
	v_fma_mix_f32 v71, v26, v184, v71 op_sel:[0,1,0] op_sel_hi:[0,1,0]
	v_fma_mix_f32 v72, v26, v185, v72 op_sel_hi:[0,1,0]
	v_fma_mix_f32 v73, v26, v185, v73 op_sel:[0,1,0] op_sel_hi:[0,1,0]
	v_fma_mix_f32 v74, v26, v186, v74 op_sel_hi:[0,1,0]
	v_fma_mix_f32 v75, v26, v186, v75 op_sel:[0,1,0] op_sel_hi:[0,1,0]
	v_fma_mix_f32 v76, v26, v187, v76 op_sel_hi:[0,1,0]
	v_fma_mix_f32 v77, v26, v187, v77 op_sel:[0,1,0] op_sel_hi:[0,1,0]
	s_waitcnt lgkmcnt(1)
	v_fma_mix_f32 v70, v25, v188, v70 op_sel_hi:[0,1,0]
	v_fma_mix_f32 v71, v25, v188, v71 op_sel:[0,1,0] op_sel_hi:[0,1,0]
	v_fma_mix_f32 v72, v25, v189, v72 op_sel_hi:[0,1,0]
	v_fma_mix_f32 v73, v25, v189, v73 op_sel:[0,1,0] op_sel_hi:[0,1,0]
	v_fma_mix_f32 v74, v25, v190, v74 op_sel_hi:[0,1,0]
	v_fma_mix_f32 v75, v25, v190, v75 op_sel:[0,1,0] op_sel_hi:[0,1,0]
	v_fma_mix_f32 v76, v25, v191, v76 op_sel_hi:[0,1,0]
	v_fma_mix_f32 v77, v25, v191, v77 op_sel:[0,1,0] op_sel_hi:[0,1,0]
	s_waitcnt lgkmcnt(0)
	v_fma_mix_f32 v70, v24, v108, v70 op_sel_hi:[0,1,0]
	v_fma_mix_f32 v71, v24, v108, v71 op_sel:[0,1,0] op_sel_hi:[0,1,0]
	v_fma_mix_f32 v72, v24, v109, v72 op_sel_hi:[0,1,0]
	v_fma_mix_f32 v73, v24, v109, v73 op_sel:[0,1,0] op_sel_hi:[0,1,0]
	v_fma_mix_f32 v74, v24, v110, v74 op_sel_hi:[0,1,0]
	v_fma_mix_f32 v75, v24, v110, v75 op_sel:[0,1,0] op_sel_hi:[0,1,0]
	v_fma_mix_f32 v76, v24, v111, v76 op_sel_hi:[0,1,0]
	v_fma_mix_f32 v77, v24, v111, v77 op_sel:[0,1,0] op_sel_hi:[0,1,0]
	v_mov_b32_e32 v26, v70
	v_mov_b32_e32 v27, v71
	v_mov_b32_e32 v62, v72
	v_mov_b32_e32 v63, v73
	v_mov_b32_e32 v65, v74
	v_mov_b32_e32 v64, v75
	v_mov_b32_e32 v66, v76
	v_mov_b32_e32 v24, v77
	v_add_f32_dpp v26, v26, v26 quad_perm:[1,0,3,2] row_mask:0xf bank_mask:0xf bound_ctrl:1
	v_add_f32_dpp v27, v27, v27 quad_perm:[1,0,3,2] row_mask:0xf bank_mask:0xf bound_ctrl:1
	v_add_f32_dpp v62, v62, v62 quad_perm:[1,0,3,2] row_mask:0xf bank_mask:0xf bound_ctrl:1
	v_add_f32_dpp v63, v63, v63 quad_perm:[1,0,3,2] row_mask:0xf bank_mask:0xf bound_ctrl:1
	v_add_f32_dpp v65, v65, v65 quad_perm:[1,0,3,2] row_mask:0xf bank_mask:0xf bound_ctrl:1
	v_add_f32_dpp v64, v64, v64 quad_perm:[1,0,3,2] row_mask:0xf bank_mask:0xf bound_ctrl:1
	v_add_f32_dpp v66, v66, v66 quad_perm:[1,0,3,2] row_mask:0xf bank_mask:0xf bound_ctrl:1
	v_add_f32_dpp v24, v24, v24 quad_perm:[1,0,3,2] row_mask:0xf bank_mask:0xf bound_ctrl:1
	v_add_f32_dpp v26, v26, v26 quad_perm:[2,3,0,1] row_mask:0xf bank_mask:0xf bound_ctrl:1
	v_add_f32_dpp v27, v27, v27 quad_perm:[2,3,0,1] row_mask:0xf bank_mask:0xf bound_ctrl:1
	v_add_f32_dpp v62, v62, v62 quad_perm:[2,3,0,1] row_mask:0xf bank_mask:0xf bound_ctrl:1
	v_add_f32_dpp v63, v63, v63 quad_perm:[2,3,0,1] row_mask:0xf bank_mask:0xf bound_ctrl:1
	v_add_f32_dpp v65, v65, v65 quad_perm:[2,3,0,1] row_mask:0xf bank_mask:0xf bound_ctrl:1
	v_add_f32_dpp v64, v64, v64 quad_perm:[2,3,0,1] row_mask:0xf bank_mask:0xf bound_ctrl:1
	v_add_f32_dpp v66, v66, v66 quad_perm:[2,3,0,1] row_mask:0xf bank_mask:0xf bound_ctrl:1
	v_add_f32_dpp v24, v24, v24 quad_perm:[2,3,0,1] row_mask:0xf bank_mask:0xf bound_ctrl:1
	v_add_f32_dpp v26, v26, v26 row_half_mirror row_mask:0xf bank_mask:0xf bound_ctrl:1
	v_add_f32_dpp v27, v27, v27 row_half_mirror row_mask:0xf bank_mask:0xf bound_ctrl:1
	v_add_f32_dpp v62, v62, v62 row_half_mirror row_mask:0xf bank_mask:0xf bound_ctrl:1
	v_add_f32_dpp v63, v63, v63 row_half_mirror row_mask:0xf bank_mask:0xf bound_ctrl:1
	v_add_f32_dpp v65, v65, v65 row_half_mirror row_mask:0xf bank_mask:0xf bound_ctrl:1
	v_add_f32_dpp v64, v64, v64 row_half_mirror row_mask:0xf bank_mask:0xf bound_ctrl:1
	v_add_f32_dpp v66, v66, v66 row_half_mirror row_mask:0xf bank_mask:0xf bound_ctrl:1
	v_add_f32_dpp v24, v24, v24 row_half_mirror row_mask:0xf bank_mask:0xf bound_ctrl:1
	v_add_f32_dpp v26, v26, v26 row_mirror row_mask:0xf bank_mask:0xf bound_ctrl:1
	v_add_f32_dpp v27, v27, v27 row_mirror row_mask:0xf bank_mask:0xf bound_ctrl:1
	v_add_f32_dpp v62, v62, v62 row_mirror row_mask:0xf bank_mask:0xf bound_ctrl:1
	v_add_f32_dpp v63, v63, v63 row_mirror row_mask:0xf bank_mask:0xf bound_ctrl:1
	v_add_f32_dpp v65, v65, v65 row_mirror row_mask:0xf bank_mask:0xf bound_ctrl:1
	v_add_f32_dpp v64, v64, v64 row_mirror row_mask:0xf bank_mask:0xf bound_ctrl:1
	v_add_f32_dpp v66, v66, v66 row_mirror row_mask:0xf bank_mask:0xf bound_ctrl:1
	v_add_f32_dpp v24, v24, v24 row_mirror row_mask:0xf bank_mask:0xf bound_ctrl:1
	v_mov_b32_e32 v100, 0
	v_mov_b32_e32 v101, 0
	v_mov_b32_e32 v102, 0
	v_mov_b32_e32 v103, 0
	v_mov_b32_e32 v104, 0
	v_mov_b32_e32 v105, 0
	v_mov_b32_e32 v106, 0
	v_mov_b32_e32 v107, 0
	v_mov_b32_dpp v100, v26 row_bcast:15 row_mask:0xa bank_mask:0xf
	v_mov_b32_dpp v101, v27 row_bcast:15 row_mask:0xa bank_mask:0xf
	v_mov_b32_dpp v102, v62 row_bcast:15 row_mask:0xa bank_mask:0xf
	v_mov_b32_dpp v103, v63 row_bcast:15 row_mask:0xa bank_mask:0xf
	v_mov_b32_dpp v104, v65 row_bcast:15 row_mask:0xa bank_mask:0xf
	v_mov_b32_dpp v105, v64 row_bcast:15 row_mask:0xa bank_mask:0xf
	v_mov_b32_dpp v106, v66 row_bcast:15 row_mask:0xa bank_mask:0xf
	v_mov_b32_dpp v107, v24 row_bcast:15 row_mask:0xa bank_mask:0xf
	v_add_f32_e32 v26, v26, v100
	v_add_f32_e32 v27, v27, v101
	v_add_f32_e32 v62, v62, v102
	v_add_f32_e32 v63, v63, v103
	v_add_f32_e32 v65, v65, v104
	v_add_f32_e32 v64, v64, v105
	v_add_f32_e32 v66, v66, v106
	v_add_f32_e32 v24, v24, v107
	v_mov_b32_e32 v100, 0
	v_mov_b32_e32 v101, 0
	v_mov_b32_e32 v102, 0
	v_mov_b32_e32 v103, 0
	v_mov_b32_e32 v104, 0
	v_mov_b32_e32 v105, 0
	v_mov_b32_e32 v106, 0
	v_mov_b32_e32 v107, 0
	v_mov_b32_dpp v100, v26 row_bcast:31 row_mask:0xc bank_mask:0xf
	v_mov_b32_dpp v101, v27 row_bcast:31 row_mask:0xc bank_mask:0xf
	v_mov_b32_dpp v102, v62 row_bcast:31 row_mask:0xc bank_mask:0xf
	v_mov_b32_dpp v103, v63 row_bcast:31 row_mask:0xc bank_mask:0xf
	v_mov_b32_dpp v104, v65 row_bcast:31 row_mask:0xc bank_mask:0xf
	v_mov_b32_dpp v105, v64 row_bcast:31 row_mask:0xc bank_mask:0xf
	v_mov_b32_dpp v106, v66 row_bcast:31 row_mask:0xc bank_mask:0xf
	v_mov_b32_dpp v107, v24 row_bcast:31 row_mask:0xc bank_mask:0xf
	v_add_f32_e32 v26, v26, v100
	v_add_f32_e32 v27, v27, v101
	v_add_f32_e32 v62, v62, v102
	v_add_f32_e32 v63, v63, v103
	v_add_f32_e32 v65, v65, v104
	v_add_f32_e32 v64, v64, v105
	v_add_f32_e32 v66, v66, v106
	v_add_f32_e32 v24, v24, v107
	v_readlane_b32 s4, v26, 63
	v_readlane_b32 s5, v27, 63
	v_readlane_b32 s6, v62, 63
	v_readlane_b32 s7, v63, 63
	v_readlane_b32 s8, v65, 63
	v_readlane_b32 s9, v64, 63
	v_readlane_b32 s10, v66, 63
	v_readlane_b32 s11, v24, 63
	s_and_saveexec_b64 s[82:83], s[2:3]
	s_cbranch_execz .LBB0_2144
; __device__ __forceinline__ void router_ph(const int WID_, const bf16* __restrict__ x3, const float* __restrict__ nw, const float* __restrict__ wrg, const float* __restrict__ brg, ...
;     ...
;         for (int i = 0; i < 8; ++i) l2[i] = wave_sum(l2[i]) + bre_l[grp * 8 + i];
;         int i0 = 0; float v0 = l2[0];
; #pragma unroll
;         for (int i = 1; i < 8; ++i) if (l2[i] > v0) { v0 = l2[i]; i0 = i; }
;         int i1 = -1; float v1 = -3.0e38f;
; #pragma unroll
;         for (int i = 0; i < 8; ++i) if (i != i0 && l2[i] > v1) { v1 = l2[i]; i1 = i; }
;         const float e1 = __expf(v1 - v0), inv = 1.f / (1.f + e1);
;         if (lane == 0) {
;             const int ea = grp * 8 + i0, eb = grp * 8 + i1;
;             mb.tok_e[2 * m] = ea; mb.tok_e[2 * m + 1] = eb; mb.tok_rs[m] = rs;
;             mb.tok_g[2 * m] = g1 * inv; mb.tok_g[2 * m + 1] = g1 * e1 * inv;
;             atomicAdd(&lcnt[ea], 1); atomicAdd(&lcnt[eb], 1);
	s_mul_i32 s12, s49, 0xffffc020
	s_add_i32 s48, s48, s12
	v_mov_b32_e32 v62, s48
	ds_read_b128 v[24:27], v62 offset:128
	ds_read_b128 v[62:65], v62 offset:144
	s_waitcnt lgkmcnt(1)
	v_pk_add_f32 v[24:25], s[4:5], v[24:25]
	s_nop 0
	v_cmp_gt_f32_e64 s[4:5], v25, v24
	v_add_f32_e32 v26, s6, v26
	v_add_f32_e32 v27, s7, v27
	v_cndmask_b32_e64 v66, v24, v25, s[4:5]
	v_cmp_gt_f32_e64 s[6:7], v26, v66
	s_waitcnt lgkmcnt(0)
	v_add_f32_e32 v63, s9, v63
	v_add_f32_e32 v62, s8, v62
	v_cndmask_b32_e64 v66, v66, v26, s[6:7]
	v_cmp_gt_f32_e64 s[8:9], v27, v66
	v_add_f32_e32 v65, s11, v65
	v_add_f32_e32 v64, s10, v64
	v_cndmask_b32_e64 v66, v66, v27, s[8:9]
	v_cmp_gt_f32_e64 s[10:11], v62, v66
	v_cndmask_b32_e64 v67, 0, 1, s[4:5]
	s_nop 0
	v_cndmask_b32_e64 v66, v66, v62, s[10:11]
	v_cmp_gt_f32_e64 s[12:13], v63, v66
	s_nop 1
	v_cndmask_b32_e64 v66, v66, v63, s[12:13]
	v_cmp_gt_f32_e64 s[14:15], v64, v66
	s_nop 1
	v_cndmask_b32_e64 v66, v66, v64, s[14:15]
	v_cmp_ngt_f32_e64 s[16:17], v65, v66
	s_and_b64 s[22:23], s[14:15], s[16:17]
	s_and_b64 s[4:5], s[6:7], exec
	v_readfirstlane_b32 s4, v67
	s_cselect_b32 s6, 2, s4
	s_and_b64 s[4:5], s[8:9], exec
	s_cselect_b32 s6, 3, s6
	s_and_b64 s[4:5], s[10:11], exec
	s_cselect_b32 s6, 4, s6
	s_and_b64 s[4:5], s[12:13], exec
	s_cselect_b32 s6, 5, s6
	s_and_b64 s[4:5], s[14:15], exec
	s_cselect_b32 s6, 6, s6
	s_and_b64 s[4:5], s[16:17], exec
	s_cselect_b32 s46, s6, 7
	s_cmp_lg_u32 s46, 5
	s_cselect_b64 s[20:21], -1, 0
	s_cmp_lg_u32 s46, 4
	s_cselect_b64 s[14:15], -1, 0
	s_cmp_lg_u32 s46, 3
	s_cselect_b64 s[12:13], -1, 0
	s_cmp_lg_u32 s46, 2
	s_cselect_b64 s[10:11], -1, 0
	s_cmp_lg_u32 s46, 1
	s_cselect_b64 s[8:9], -1, 0
	s_cmp_eq_u32 s46, 0
	s_cselect_b64 s[6:7], -1, 0
	v_cmp_nlt_f32_e64 s[4:5], s34, v24
	s_or_b64 s[4:5], s[6:7], s[4:5]
	s_nop 0
	v_cndmask_b32_e64 v24, v24, v197, s[4:5]
	v_cmp_gt_f32_e64 s[6:7], v25, v24
	s_and_b64 s[6:7], s[8:9], s[6:7]
	s_nop 0
	v_cndmask_b32_e64 v24, v24, v25, s[6:7]
	v_cmp_gt_f32_e64 s[8:9], v26, v24
	s_and_b64 s[8:9], s[10:11], s[8:9]
	v_cndmask_b32_e64 v25, 0, -1, s[4:5]
	v_cndmask_b32_e64 v24, v24, v26, s[8:9]
	v_cndmask_b32_e32 v26, v61, v60, vcc
	v_sub_f32_e32 v22, v22, v26
	v_mul_f32_e32 v22, 0x3fb8aa3b, v22
	v_sub_f32_e32 v23, v23, v26
	v_exp_f32_e32 v22, v22
	v_mul_f32_e32 v23, 0x3fb8aa3b, v23
	v_exp_f32_e32 v23, v23
	v_cmp_gt_f32_e64 s[10:11], v27, v24
	s_and_b64 s[10:11], s[12:13], s[10:11]
	v_add_f32_e32 v22, 0, v22
	v_cndmask_b32_e64 v24, v24, v27, s[10:11]
	v_cmp_gt_f32_e64 s[12:13], v62, v24
	v_add_f32_e32 v22, v23, v22
	v_sub_f32_e32 v23, v59, v26
	s_and_b64 s[12:13], s[14:15], s[12:13]
	v_mul_f32_e32 v23, 0x3fb8aa3b, v23
	v_cndmask_b32_e64 v24, v24, v62, s[12:13]
	v_exp_f32_e32 v23, v23
	v_cmp_gt_f32_e64 s[14:15], v63, v24
	s_and_b64 s[14:15], s[20:21], s[14:15]
	v_add_f32_e32 v22, v23, v22
	v_cndmask_b32_e64 v24, v24, v63, s[14:15]
	v_cmp_ngt_f32_e64 s[20:21], v64, v24
	v_sub_f32_e32 v23, v60, v26
	s_or_b64 s[20:21], s[22:23], s[20:21]
	v_mul_f32_e32 v23, 0x3fb8aa3b, v23
	v_cndmask_b32_e64 v24, v64, v24, s[20:21]
	v_exp_f32_e32 v23, v23
	v_cmp_gt_f32_e64 s[22:23], v65, v24
	s_and_b64 s[22:23], s[16:17], s[22:23]
	s_and_b64 s[4:5], s[6:7], exec
	v_readfirstlane_b32 s4, v25
	v_add_f32_e32 v22, v23, v22
	s_cselect_b32 s6, 1, s4
	v_div_scale_f32 v23, s[4:5], v22, v22, 1.0
	v_rcp_f32_e32 v26, v23
	v_cndmask_b32_e64 v24, v24, v65, s[22:23]
	v_cndmask_b32_e64 v25, v65, v66, s[16:17]
	s_and_b64 s[4:5], s[8:9], exec
	v_fma_f32 v27, -v23, v26, 1.0
	v_fmac_f32_e32 v26, v27, v26
	v_div_scale_f32 v27, vcc, 1.0, v22, 1.0
	v_mul_f32_e32 v59, v27, v26
	v_fma_f32 v60, -v23, v59, v27
	v_fmac_f32_e32 v59, v60, v26
	v_fma_f32 v23, -v23, v59, v27
	v_div_fmas_f32 v23, v23, v26, v59
	v_div_fixup_f32 v26, v23, v22, 1.0
	v_sub_f32_e32 v22, v24, v25
	v_mul_f32_e32 v22, 0x3fb8aa3b, v22
	v_exp_f32_e32 v24, v22
	s_cselect_b32 s6, 2, s6
	s_and_b64 s[4:5], s[10:11], exec
	s_cselect_b32 s6, 3, s6
	v_add_f32_e32 v22, 1.0, v24
	v_div_scale_f32 v23, s[4:5], v22, v22, 1.0
	v_rcp_f32_e32 v25, v23
	s_and_b64 s[4:5], s[12:13], exec
	s_cselect_b32 s6, 4, s6
	s_and_b64 s[4:5], s[14:15], exec
	s_cselect_b32 s6, 5, s6
	s_and_b64 s[4:5], s[20:21], exec
	v_fma_f32 v27, -v23, v25, 1.0
	s_cselect_b32 s6, s6, 6
	s_and_b64 s[4:5], s[22:23], exec
	v_fmac_f32_e32 v25, v27, v25
	v_div_scale_f32 v27, vcc, 1.0, v22, 1.0
	s_cselect_b32 s8, 7, s6
	v_mul_f32_e32 v59, v27, v25
	s_lshl_b32 s4, s49, 3
	s_ashr_i32 s81, s80, 31
	v_fma_f32 v60, -v23, v59, v27
	s_or_b32 s9, s46, s4
	s_add_i32 s12, s8, s4
	s_lshl_b64 s[4:5], s[80:81], 2
	v_fmac_f32_e32 v59, v60, v25
	s_add_u32 s6, s52, s4
	v_fma_f32 v23, -v23, v59, v27
	s_addc_u32 s7, s53, s5
	s_add_i32 s10, s80, 1
	v_div_fmas_f32 v23, v23, v25, v59
	s_ashr_i32 s11, s10, 31
	v_div_fixup_f32 v25, v23, v22, 1.0
	v_mov_b32_e32 v22, s9
	v_mov_b32_e32 v23, s12
	s_add_u32 s4, s40, s4
	global_store_dwordx2 v129, v[22:23], s[6:7]
	global_store_dword v129, v2, s[78:79]
	v_mul_f32_e32 v2, v26, v25
	s_addc_u32 s5, s41, s5
	global_store_dword v129, v2, s[4:5]
	s_lshl_b64 s[4:5], s[10:11], 2
	v_mul_f32_e32 v2, v26, v24
	s_add_u32 s4, s40, s4
	v_mul_f32_e32 v2, v2, v25
	s_addc_u32 s5, s41, s5
	global_store_dword v129, v2, s[4:5]
	s_waitcnt vmcnt(4)
	s_mov_b64 s[4:5], exec
	v_mbcnt_lo_u32_b32 v2, s4, 0
	v_mbcnt_hi_u32_b32 v2, s5, v2
	v_cmp_eq_u32_e32 vcc, 0, v2
	s_and_saveexec_b64 s[6:7], vcc
	s_cbranch_execz .LBB0_2148
	s_lshl_b32 s9, s9, 2
	s_add_i32 s9, s9, 0
	s_bcnt1_i32_b64 s4, s[4:5]
	v_mov_b32_e32 v2, s9
	v_mov_b32_e32 v22, s4
	ds_add_u32 v2, v22
